# attention unit prologue: bound/threshold loads issued together, forget-bias staging loads all in flight before LDS stores
# baseline (speedup 1.0000x reference)
; template<int THRL> __device__ __forceinline__ void attn_unit(int b,int h,int qb,const bf16*Q,const bf16*__restrict__ K,const bf16*__restrict__ V,bf16*O,const float*__restrict__ F2g,const float*__restrict__ gain,float qkb,char*shm){
;     ...
;   { const int NTf=(q0+QB)/KVBLK; const float thr=f2row[q0]+qkb+40.0f; const int ta=lane,tb=lane+64;
;     const bool va=(ta<NTf-4)&&(f2row[64*ta+63]>thr), vb=(tb<NTf-4)&&(f2row[64*tb+63]>thr);
;     t0=(__builtin_popcountll(__ballot(va))+__builtin_popcountll(__ballot(vb)))&~1; t0=__builtin_amdgcn_readfirstlane(t0); }
; __global__ void __launch_bounds__(NWAVES * 64, 2) mega_fwd(Args args) {
;     ...
;                 if (idx < 512) { const attn_body::AttnUnit u{(idx & 3) * 4 + 3 - ((idx >> 2) & 3), 31 - (idx >> 4)};
;                     attn_body::attn_unit<8>(u.bh / 4, u.bh % 4, u.qb, AT.Q, AT.K, AT.V, AT.O, AT.F2, AT.gain, 2.0f * sqrtf(__uint_as_float(AT.qkn[2 * u.bh]) * __uint_as_float(AT.qkn[2 * u.bh + 1])), (char*)lds); }
.LBB0_2757:
	s_or_b64 exec, exec, s[0:1]
	v_mov_b32_e32 v0, s17
	s_waitcnt vmcnt(0) lgkmcnt(0)
	s_barrier
	ds_read_b32 v0, v0
	s_mov_b64 s[0:1], -1
	s_waitcnt lgkmcnt(0)
	s_barrier
	v_readfirstlane_b32 s4, v0
	s_cmpk_gt_i32 s4, 0x1ff
	s_cbranch_scc1 .LBB0_2752
	s_lshl_b32 s0, s4, 2
	s_and_b32 s0, s0, 12
	s_or_b32 s0, s0, 3
	s_bfe_u32 s1, s4, 0x20002
	s_sub_i32 s0, s0, s1
	s_lshr_b32 s55, s0, 2
	s_and_b32 s28, s0, 3
	s_lshl_b32 s0, s0, 3
	v_mov_b32_e32 v0, s0
	global_load_dwordx2 v[0:1], v0, s[6:7]
	s_lshl_b32 s78, s4, 4
	s_and_b32 s78, s78, 0xffffff00
	s_sub_i32 s78, 0x1f00, s78
	s_lshl_b32 s74, s55, 17
	s_add_u32 s74, s45, s74
	s_addc_u32 s75, s47, 0
	s_lshl_b32 s79, s28, 15
	s_add_u32 s74, s74, s79
	s_addc_u32 s75, s75, 0
	s_lshl_b32 s78, s78, 2
	s_add_u32 s76, s74, s78
	s_addc_u32 s77, s75, 0
	v_and_b32_e32 v9, 63, v228
	v_lshlrev_b32_e32 v9, 8, v9
	global_load_dword v6, v3, s[76:77]
	global_load_dword v7, v9, s[74:75] offset:252
	v_or_b32_e32 v9, 0x4000, v9
	global_load_dword v8, v9, s[74:75] offset:252
	s_mov_b32 s0, 0xf800000
	v_mov_b32_e32 v50, v228
	s_mov_b64 s[24:25], 0
	v_and_b32_e32 v131, 63, v50
	v_readfirstlane_b32 s35, v50
	s_waitcnt vmcnt(0)
	v_mul_f32_e32 v0, v0, v1
	v_cmp_gt_f32_e32 vcc, s0, v0
	v_mul_f32_e32 v1, 0x4f800000, v0
	s_nop 0
	v_cndmask_b32_e32 v0, v0, v1, vcc
	v_sqrt_f32_e32 v1, v0
	s_nop 0
	v_add_u32_e32 v2, -1, v1
	v_fma_f32 v4, -v2, v1, v0
	v_cmp_ge_f32_e64 s[0:1], 0, v4
	v_add_u32_e32 v4, 1, v1
	s_nop 0
	v_cndmask_b32_e64 v2, v1, v2, s[0:1]
	v_fma_f32 v1, -v4, v1, v0
	v_cmp_lt_f32_e64 s[0:1], 0, v1
	s_nop 1
	v_cndmask_b32_e64 v1, v2, v4, s[0:1]
	s_lshl_b32 s0, s4, 4
	s_and_b32 s29, s0, 0xffffff00
	s_sub_i32 s52, 0x1f00, s29
	s_lshl_b32 s0, s55, 17
	s_add_u32 s0, s45, s0
	s_addc_u32 s1, s47, 0
	s_lshl_b32 s4, s28, 15
	s_add_u32 s0, s0, s4
	s_addc_u32 s1, s1, 0
	s_sub_i32 s4, 0x2000, s29
	v_mul_f32_e32 v2, 0x37800000, v1
	s_lshr_b32 s30, s4, 6
	s_lshl_b64 s[4:5], s[52:53], 2
	v_cndmask_b32_e32 v1, v1, v2, vcc
	v_mov_b32_e32 v2, 0x260
	s_add_u32 s4, s0, s4
	v_cmp_class_f32_e32 vcc, v0, v2
	s_addc_u32 s5, s1, s5
	s_add_i32 s31, s30, -4
	v_cndmask_b32_e32 v0, v1, v0, vcc
	v_mov_b32_e32 v1, v6
	v_cmp_gt_u32_e32 vcc, s31, v131
	s_mov_b64 s[4:5], 0
	s_waitcnt vmcnt(0)
	v_fmac_f32_e32 v1, 2.0, v0
	v_add_f32_e32 v1, 0x42200000, v1
	s_and_saveexec_b64 s[26:27], vcc
	s_cbranch_execz .LBB0_2760
	v_lshlrev_b32_e32 v0, 8, v131
	v_mov_b32_e32 v0, v7
	s_waitcnt vmcnt(0)
	v_cmp_gt_f32_e32 vcc, v0, v1
	s_and_b64 s[24:25], vcc, exec
.LBB0_2760:
	s_or_b64 exec, exec, s[26:27]
	v_or_b32_e32 v2, 64, v131
	v_cmp_gt_u32_e32 vcc, s31, v2
	s_and_saveexec_b64 s[26:27], vcc
	s_cbranch_execz .LBB0_2762
	v_lshlrev_b32_e32 v0, 8, v2
	v_mov_b32_e32 v0, v8
	s_waitcnt vmcnt(0)
	v_cmp_gt_f32_e32 vcc, v0, v1
	s_and_b64 s[4:5], vcc, exec

; template<int THRL> __device__ __forceinline__ void attn_unit(int b,int h,int qb,const bf16*Q,const bf16*__restrict__ K,const bf16*__restrict__ V,bf16*O,const float*__restrict__ F2g,const float*__restrict__ gain,float qkb,char*shm){
;     ...
;   { const float*f2src=f2row+(long)t0*KVBLK; __attribute__((address_space(3))) float*f2l=(__attribute__((address_space(3))) float*)(shm3+LDS_F2);
;     for(int i=tid;i<NT*KVBLK/4;i+=NW*64){ const f32x4_t v=*(const f32x4_t*)(f2src+4*i); *(__attribute__((address_space(3))) f32x4_t*)(f2l+4*i)=v; } }
.LBB0_2764:
	s_mov_b64 s[92:93], exec
	s_mov_b64 s[88:89], 0x2000
	v_ashrrev_i32_e32 v5, 31, v4
	v_lshl_add_u64 v[6:7], v[4:5], 2, s[0:1]
	global_load_dwordx4 v[10:13], v[6:7], off
	v_add_u32_e32 v2, 0x200, v2
	v_cmp_gt_i32_e32 vcc, s27, v2
	s_and_b64 exec, exec, vcc
	s_mov_b64 s[94:95], exec
	v_lshl_add_u64 v[6:7], v[6:7], 0, s[88:89]
	global_load_dwordx4 v[14:17], v[6:7], off
	v_add_u32_e32 v2, 0x200, v2
	v_cmp_gt_i32_e32 vcc, s27, v2
	s_and_b64 exec, exec, vcc
	s_mov_b64 s[98:99], exec
	v_lshl_add_u64 v[6:7], v[6:7], 0, s[88:89]
	global_load_dwordx4 v[18:21], v[6:7], off
	v_add_u32_e32 v2, 0x200, v2
	v_cmp_gt_i32_e32 vcc, s27, v2
	s_and_b64 exec, exec, vcc
	v_lshl_add_u64 v[6:7], v[6:7], 0, s[88:89]
	global_load_dwordx4 v[22:25], v[6:7], off
	s_waitcnt vmcnt(0)
	ds_write_b128 v1, v[22:25] offset:24576
	s_mov_b64 exec, s[98:99]
	ds_write_b128 v1, v[18:21] offset:16384
	s_mov_b64 exec, s[94:95]
	ds_write_b128 v1, v[14:17] offset:8192
	s_mov_b64 exec, s[92:93]
	ds_write_b128 v1, v[10:13]
